# P1 prologue: scalar pointer loads, 3 param loads issued together ahead of the DMA, LDS park moved behind first vmcnt
# baseline (speedup 1.0000x reference)
.LBB0_20:
	v_lshlrev_b32_e32 v34, 4, v72
	v_lshl_or_b32 v1, v1, 13, v34
	ds_write_b128 v1, v[6:9]
	ds_write_b128 v1, v[10:13] offset:1024
	ds_write_b128 v1, v[14:17] offset:2048
	ds_write_b128 v1, v[18:21] offset:3072
	ds_write_b128 v1, v[22:25] offset:4096
	ds_write_b128 v1, v[26:29] offset:5120
	ds_write_b128 v1, v[30:33] offset:6144
	ds_write_b128 v1, v[2:5] offset:7168
	v_lshlrev_b32_e32 v32, 5, v0
	s_ashr_i32 s3, s2, 31
	s_waitcnt lgkmcnt(0)
	s_barrier
	ds_read_b128 v[0:3], v32
	ds_read_b128 v[4:7], v32 offset:16
	ds_read_b128 v[8:11], v32 offset:8192
	ds_read_b128 v[12:15], v32 offset:8208
	ds_read_b128 v[16:19], v32 offset:16384
	ds_read_b128 v[20:23], v32 offset:16400
	ds_read_b128 v[24:27], v32 offset:24576
	ds_read_b128 v[28:31], v32 offset:24592
	s_lshl_b64 s[0:1], s[2:3], 13
	s_add_u32 s0, s12, s0
	s_addc_u32 s1, s13, s1
	v_mov_b32_e32 v33, 0
	v_lshl_add_u64 v[32:33], s[0:1], 0, v[32:33]
	s_mov_b64 s[0:1], 0xd400000
	v_lshl_add_u64 v[34:35], v[32:33], 0, s[0:1]
	s_waitcnt lgkmcnt(5)
	v_pk_add_f32 v[2:3], v[2:3], v[10:11]
	v_pk_add_f32 v[0:1], v[0:1], v[8:9]
	s_waitcnt lgkmcnt(1)
	v_pk_add_f32 v[8:9], v[18:19], v[26:27]
	s_mov_b32 s0, 0xd400000
	v_pk_add_f32 v[10:11], v[16:17], v[24:25]
	v_pk_add_f32 v[2:3], v[2:3], v[8:9]
	v_add_co_u32_e32 v8, vcc, s0, v32
	v_pk_add_f32 v[0:1], v[0:1], v[10:11]
	s_nop 0
	v_addc_co_u32_e32 v9, vcc, 0, v33, vcc
	global_store_dwordx4 v[8:9], v[0:3], off
	v_pk_add_f32 v[4:5], v[4:5], v[12:13]
	s_nop 0
	v_pk_add_f32 v[0:1], v[6:7], v[14:15]
	s_waitcnt lgkmcnt(0)
	v_pk_add_f32 v[2:3], v[22:23], v[30:31]
	v_pk_add_f32 v[6:7], v[20:21], v[28:29]
	v_pk_add_f32 v[2:3], v[0:1], v[2:3]
	v_pk_add_f32 v[0:1], v[4:5], v[6:7]
	global_store_dwordx4 v[34:35], v[0:3], off offset:16
	s_endpgm
	.p2align	8

.LBB1_22:
	s_load_dwordx2 s[4:5], s[0:1], 0x8
	s_lshl_b32 s0, s2, 8
	s_and_b32 s0, s0, 0x700
	v_or_b32_e32 v0, s0, v0
	s_lshl_b32 s0, s2, 3
	s_and_b32 s2, s0, 0xffffffc0
	s_ashr_i32 s3, s2, 31
	s_lshl_b64 s[0:1], s[2:3], 2
	s_waitcnt lgkmcnt(0)
	s_add_u32 s8, s6, s0
	s_addc_u32 s9, s7, s1
	s_add_u32 s0, s8, 0xd01a000
	s_addc_u32 s1, s9, 0
	s_mul_hi_i32 s3, s2, 0x6000
	s_mulk_i32 s2, 0x6000
	s_add_u32 s2, s4, s2
	v_mov_b32_e32 v33, 0
	s_addc_u32 s3, s5, s3
	v_lshlrev_b32_e32 v32, 2, v0
	v_lshl_add_u64 v[34:35], s[2:3], 0, v[32:33]
	v_mov_b32_e32 v0, 0xd01a000
	s_movk_i32 s2, 0x4000
	global_load_dwordx4 v[4:7], v33, s[0:1] offset:32
	global_load_dwordx4 v[8:11], v33, s[0:1] offset:16
	global_load_dwordx4 v[12:15], v0, s[8:9]
	v_add_co_u32_e32 v0, vcc, s2, v34
	s_mov_b32 s2, 0xa000
	s_nop 0
	v_addc_co_u32_e32 v1, vcc, 0, v35, vcc
	v_add_co_u32_e32 v2, vcc, s2, v34
	s_mov_b32 s2, 0x10000
	s_nop 0
	v_addc_co_u32_e32 v3, vcc, 0, v35, vcc
	v_add_co_u32_e32 v16, vcc, s2, v34
	s_mov_b32 s2, 0x16000
	s_nop 0
	v_addc_co_u32_e32 v17, vcc, 0, v35, vcc
	v_add_co_u32_e32 v18, vcc, s2, v34
	s_mov_b32 s2, 0x1c000
	s_nop 0
	v_addc_co_u32_e32 v19, vcc, 0, v35, vcc
	v_add_co_u32_e32 v20, vcc, s2, v34
	s_mov_b32 s2, 0x22000
	s_nop 0
	v_addc_co_u32_e32 v21, vcc, 0, v35, vcc
	v_add_co_u32_e32 v22, vcc, s2, v34
	s_mov_b32 s2, 0x28000
	s_nop 0
	v_addc_co_u32_e32 v23, vcc, 0, v35, vcc
	v_add_co_u32_e32 v24, vcc, s2, v34
	s_mov_b32 s2, 0x2e000
	s_nop 0
	v_addc_co_u32_e32 v25, vcc, 0, v35, vcc
	v_add_co_u32_e32 v26, vcc, s2, v34
	s_mov_b32 s2, 0x34000
	s_nop 0
	v_addc_co_u32_e32 v27, vcc, 0, v35, vcc
	global_load_dword v48, v[0:1], off nt
	global_load_dword v49, v[2:3], off nt
	global_load_dword v50, v[16:17], off nt
	global_load_dword v51, v[18:19], off nt
	global_load_dword v52, v[20:21], off nt
	global_load_dword v53, v[22:23], off nt
	global_load_dword v54, v[24:25], off nt
	global_load_dword v55, v[26:27], off nt
	v_add_co_u32_e32 v0, vcc, s2, v34
	s_mov_b32 s2, 0x3a000
	s_nop 0
	v_addc_co_u32_e32 v1, vcc, 0, v35, vcc
	v_add_co_u32_e32 v2, vcc, s2, v34
	s_mov_b32 s2, 0x40000
	s_nop 0
	v_addc_co_u32_e32 v3, vcc, 0, v35, vcc
	v_add_co_u32_e32 v36, vcc, s2, v34
	s_mov_b32 s2, 0x46000
	s_nop 0
	v_addc_co_u32_e32 v37, vcc, 0, v35, vcc
	v_add_co_u32_e32 v38, vcc, s2, v34
	s_mov_b32 s2, 0x4c000
	s_nop 0
	v_addc_co_u32_e32 v39, vcc, 0, v35, vcc
	v_add_co_u32_e32 v40, vcc, s2, v34
	s_mov_b32 s2, 0x52000
	s_nop 0
	v_addc_co_u32_e32 v41, vcc, 0, v35, vcc
	v_add_co_u32_e32 v42, vcc, s2, v34
	s_mov_b32 s2, 0x58000
	s_nop 0
	v_addc_co_u32_e32 v43, vcc, 0, v35, vcc
	v_add_co_u32_e32 v44, vcc, s2, v34
	s_mov_b32 s2, 0x5e000
	s_nop 0
	v_addc_co_u32_e32 v45, vcc, 0, v35, vcc
	v_add_co_u32_e32 v46, vcc, s2, v34
	s_mov_b32 s2, 0x64000
	s_nop 0
	v_addc_co_u32_e32 v47, vcc, 0, v35, vcc
	global_load_dword v56, v[0:1], off nt
	global_load_dword v57, v[2:3], off nt
	global_load_dword v58, v[36:37], off nt
	global_load_dword v59, v[38:39], off nt
	global_load_dword v60, v[40:41], off nt
	global_load_dword v61, v[42:43], off nt
	global_load_dword v62, v[44:45], off nt
	global_load_dword v63, v[46:47], off nt
	global_load_dwordx4 v[20:23], v33, s[0:1] offset:48
	global_load_dwordx4 v[28:31], v33, s[0:1] offset:64
	global_load_dwordx4 v[16:19], v33, s[0:1] offset:96
	global_load_dwordx4 v[24:27], v33, s[0:1] offset:80
	v_add_co_u32_e32 v0, vcc, s2, v34
	s_mov_b32 s2, 0x6a000
	s_nop 0
	v_addc_co_u32_e32 v1, vcc, 0, v35, vcc
	v_add_co_u32_e32 v2, vcc, s2, v34
	s_mov_b32 s2, 0x70000
	s_nop 0
	v_addc_co_u32_e32 v3, vcc, 0, v35, vcc
	v_add_co_u32_e32 v36, vcc, s2, v34
	s_mov_b32 s2, 0x76000
	s_nop 0
	v_addc_co_u32_e32 v37, vcc, 0, v35, vcc
	v_add_co_u32_e32 v38, vcc, s2, v34
	s_mov_b32 s2, 0x7c000
	s_nop 0
	v_addc_co_u32_e32 v39, vcc, 0, v35, vcc
	v_add_co_u32_e32 v40, vcc, s2, v34
	s_mov_b32 s2, 0x82000
	s_nop 0
	v_addc_co_u32_e32 v41, vcc, 0, v35, vcc
	v_add_co_u32_e32 v42, vcc, s2, v34
	s_mov_b32 s2, 0x88000
	s_nop 0
	v_addc_co_u32_e32 v43, vcc, 0, v35, vcc
	v_add_co_u32_e32 v44, vcc, s2, v34
	s_mov_b32 s2, 0x8e000
	s_nop 0
	v_addc_co_u32_e32 v45, vcc, 0, v35, vcc
	v_add_co_u32_e32 v46, vcc, s2, v34
	s_mov_b32 s2, 0x94000
	s_nop 0
	v_addc_co_u32_e32 v47, vcc, 0, v35, vcc
	global_load_dword v64, v[0:1], off nt
	global_load_dword v65, v[2:3], off nt
	global_load_dword v66, v[36:37], off nt
	global_load_dword v67, v[38:39], off nt
	global_load_dword v68, v[40:41], off nt
	global_load_dword v69, v[42:43], off nt
	global_load_dword v70, v[44:45], off nt
	global_load_dword v71, v[46:47], off nt
	v_add_co_u32_e32 v36, vcc, s2, v34
	s_mov_b32 s2, 0x9a000
	s_nop 0
	v_addc_co_u32_e32 v37, vcc, 0, v35, vcc
	v_add_co_u32_e32 v38, vcc, s2, v34
	s_mov_b32 s2, 0xa0000
	s_nop 0
	v_addc_co_u32_e32 v39, vcc, 0, v35, vcc
	v_add_co_u32_e32 v40, vcc, s2, v34
	s_mov_b32 s2, 0xa6000
	s_nop 0
	v_addc_co_u32_e32 v41, vcc, 0, v35, vcc
	v_add_co_u32_e32 v42, vcc, s2, v34
	s_mov_b32 s2, 0xac000
	s_nop 0
	v_addc_co_u32_e32 v43, vcc, 0, v35, vcc
	v_add_co_u32_e32 v44, vcc, s2, v34
	s_mov_b32 s2, 0xb2000
	s_nop 0
	v_addc_co_u32_e32 v45, vcc, 0, v35, vcc
	v_add_co_u32_e32 v46, vcc, s2, v34
	s_mov_b32 s2, 0xb8000
	s_nop 0
	v_addc_co_u32_e32 v47, vcc, 0, v35, vcc
	global_load_dwordx4 v[0:3], v33, s[0:1] offset:112
	global_load_dword v72, v[36:37], off nt
	global_load_dword v73, v[38:39], off nt
	global_load_dword v74, v[40:41], off nt
	global_load_dword v75, v[42:43], off nt
	global_load_dword v76, v[44:45], off nt
	global_load_dword v77, v[46:47], off nt
	s_waitcnt vmcnt(34)
	v_fma_f32 v46, v12, v48, 0
	s_waitcnt vmcnt(33)
	v_fma_f32 v47, v13, v49, 0
	s_waitcnt vmcnt(30)
	v_fmac_f32_e32 v46, v8, v52
	v_add_co_u32_e32 v8, vcc, s2, v34
	v_fma_f32 v48, v14, v50, 0
	s_waitcnt vmcnt(29)
	v_fmac_f32_e32 v47, v9, v53
	v_addc_co_u32_e32 v9, vcc, 0, v35, vcc
	s_mov_b32 s2, 0xbe000
	v_fma_f32 v49, v15, v51, 0
	s_waitcnt vmcnt(28)
	v_fmac_f32_e32 v48, v10, v54
	v_add_co_u32_e32 v10, vcc, s2, v34
	s_waitcnt vmcnt(27)
	v_fmac_f32_e32 v49, v11, v55
	s_waitcnt vmcnt(26)
	v_fmac_f32_e32 v46, v4, v56
	v_addc_co_u32_e32 v11, vcc, 0, v35, vcc
	s_mov_b32 s2, 0xc4000
	s_waitcnt vmcnt(25)
	v_fmac_f32_e32 v47, v5, v57
	s_waitcnt vmcnt(18)
	v_fmac_f32_e32 v46, v20, v60
	v_add_co_u32_e32 v20, vcc, s2, v34
	v_fmac_f32_e32 v47, v21, v61
	s_nop 0
	v_addc_co_u32_e32 v21, vcc, 0, v35, vcc
	s_mov_b32 s2, 0xca000
	v_add_co_u32_e32 v36, vcc, s2, v34
	s_mov_b32 s2, 0xd0000
	s_nop 0
	v_addc_co_u32_e32 v37, vcc, 0, v35, vcc
	v_add_co_u32_e32 v38, vcc, s2, v34
	s_mov_b32 s2, 0xd6000
	s_nop 0
	v_addc_co_u32_e32 v39, vcc, 0, v35, vcc
	v_add_co_u32_e32 v40, vcc, s2, v34
	s_mov_b32 s2, 0xdc000
	s_nop 0
	v_addc_co_u32_e32 v41, vcc, 0, v35, vcc
	v_add_co_u32_e32 v42, vcc, s2, v34
	s_mov_b32 s2, 0xe2000
	s_nop 0
	v_addc_co_u32_e32 v43, vcc, 0, v35, vcc
	s_waitcnt vmcnt(14)
	v_fmac_f32_e32 v46, v28, v64
	v_add_co_u32_e32 v44, vcc, s2, v34
	s_waitcnt vmcnt(13)
	v_fmac_f32_e32 v47, v29, v65
	s_waitcnt vmcnt(10)
	v_fmac_f32_e32 v46, v24, v68
	v_addc_co_u32_e32 v45, vcc, 0, v35, vcc
	s_waitcnt vmcnt(9)
	v_fmac_f32_e32 v47, v25, v69
	s_mov_b32 s2, 0xe8000
	v_fmac_f32_e32 v48, v6, v58
	v_fmac_f32_e32 v49, v7, v59
	global_load_dword v50, v[8:9], off nt
	global_load_dword v51, v[10:11], off nt
	global_load_dwordx4 v[4:7], v33, s[0:1] offset:128
	global_load_dwordx4 v[12:15], v33, s[0:1] offset:144
	s_nop 0
	global_load_dwordx4 v[8:11], v33, s[0:1] offset:160
	v_fmac_f32_e32 v48, v22, v62
	v_fmac_f32_e32 v49, v23, v63
	v_fmac_f32_e32 v48, v30, v66
	v_fmac_f32_e32 v49, v31, v67
	s_waitcnt vmcnt(13)
	v_fmac_f32_e32 v48, v26, v70
	s_waitcnt vmcnt(12)
	v_fmac_f32_e32 v49, v27, v71
	s_waitcnt vmcnt(10)
	v_fmac_f32_e32 v46, v16, v72
	s_waitcnt vmcnt(9)
	v_fmac_f32_e32 v47, v17, v73
	s_waitcnt vmcnt(8)
	v_fmac_f32_e32 v48, v18, v74
	s_waitcnt vmcnt(7)
	v_fmac_f32_e32 v49, v19, v75
	s_waitcnt vmcnt(6)
	v_fmac_f32_e32 v46, v0, v76
	v_add_co_u32_e32 v0, vcc, s2, v34
	s_waitcnt vmcnt(5)
	v_fmac_f32_e32 v47, v1, v77
	v_addc_co_u32_e32 v1, vcc, 0, v35, vcc
	s_mov_b32 s2, 0xee000
	v_add_co_u32_e32 v16, vcc, s2, v34
	s_mov_b32 s2, 0xf4000
	s_nop 0
	v_addc_co_u32_e32 v17, vcc, 0, v35, vcc
	global_load_dword v52, v[20:21], off nt
	global_load_dword v53, v[36:37], off nt
	global_load_dword v54, v[38:39], off nt
	global_load_dword v55, v[40:41], off nt
	global_load_dword v56, v[42:43], off nt
	global_load_dword v57, v[44:45], off nt
	global_load_dword v58, v[0:1], off nt
	global_load_dword v59, v[16:17], off nt
	v_add_co_u32_e32 v0, vcc, s2, v34
	s_mov_b32 s2, 0xfa000
	s_nop 0
	v_addc_co_u32_e32 v1, vcc, 0, v35, vcc
	v_add_co_u32_e32 v28, vcc, s2, v34
	s_mov_b32 s2, 0x100000
	s_nop 0
	v_addc_co_u32_e32 v29, vcc, 0, v35, vcc
	v_add_co_u32_e32 v30, vcc, s2, v34
	s_mov_b32 s2, 0x106000
	s_nop 0
	v_addc_co_u32_e32 v31, vcc, 0, v35, vcc
	v_add_co_u32_e32 v36, vcc, s2, v34
	s_mov_b32 s2, 0x10c000
	s_nop 0
	v_addc_co_u32_e32 v37, vcc, 0, v35, vcc
	v_add_co_u32_e32 v38, vcc, s2, v34
	s_mov_b32 s2, 0x112000
	s_nop 0
	v_addc_co_u32_e32 v39, vcc, 0, v35, vcc
	v_add_co_u32_e32 v40, vcc, s2, v34
	s_mov_b32 s2, 0x118000
	s_nop 0
	v_addc_co_u32_e32 v41, vcc, 0, v35, vcc
	v_add_co_u32_e32 v42, vcc, s2, v34
	s_mov_b32 s2, 0x11e000
	s_nop 0
	v_addc_co_u32_e32 v43, vcc, 0, v35, vcc
	v_add_co_u32_e32 v44, vcc, s2, v34
	s_mov_b32 s2, 0x124000
	s_nop 0
	v_addc_co_u32_e32 v45, vcc, 0, v35, vcc
	global_load_dword v60, v[0:1], off nt
	global_load_dword v61, v[28:29], off nt
	global_load_dword v62, v[30:31], off nt
	global_load_dword v63, v[36:37], off nt
	global_load_dword v64, v[38:39], off nt
	global_load_dword v65, v[40:41], off nt
	global_load_dword v66, v[42:43], off nt
	global_load_dword v67, v[44:45], off nt
	global_load_dwordx4 v[16:19], v33, s[0:1] offset:208
	global_load_dwordx4 v[20:23], v33, s[0:1] offset:176
	global_load_dwordx4 v[24:27], v33, s[0:1] offset:192
	v_add_co_u32_e32 v0, vcc, s2, v34
	s_mov_b32 s2, 0x12a000
	s_nop 0
	v_addc_co_u32_e32 v1, vcc, 0, v35, vcc
	v_add_co_u32_e32 v28, vcc, s2, v34
	s_mov_b32 s2, 0x130000
	s_nop 0
	v_addc_co_u32_e32 v29, vcc, 0, v35, vcc
	v_add_co_u32_e32 v30, vcc, s2, v34
	s_mov_b32 s2, 0x136000
	s_nop 0
	v_addc_co_u32_e32 v31, vcc, 0, v35, vcc
	v_add_co_u32_e32 v36, vcc, s2, v34
	s_mov_b32 s2, 0x13c000
	s_nop 0
	v_addc_co_u32_e32 v37, vcc, 0, v35, vcc
	v_add_co_u32_e32 v38, vcc, s2, v34
	s_mov_b32 s2, 0x142000
	s_nop 0
	v_addc_co_u32_e32 v39, vcc, 0, v35, vcc
	v_add_co_u32_e32 v40, vcc, s2, v34
	s_mov_b32 s2, 0x148000
	s_nop 0
	v_addc_co_u32_e32 v41, vcc, 0, v35, vcc
	v_add_co_u32_e32 v42, vcc, s2, v34
	s_mov_b32 s2, 0x14e000
	s_nop 0
	v_addc_co_u32_e32 v43, vcc, 0, v35, vcc
	v_add_co_u32_e32 v44, vcc, s2, v34
	s_mov_b32 s2, 0x154000
	s_nop 0
	v_addc_co_u32_e32 v45, vcc, 0, v35, vcc
	global_load_dword v68, v[0:1], off nt
	global_load_dword v69, v[28:29], off nt
	global_load_dword v70, v[30:31], off nt
	global_load_dword v71, v[36:37], off nt
	global_load_dword v72, v[38:39], off nt
	global_load_dword v73, v[40:41], off nt
	global_load_dword v74, v[42:43], off nt
	global_load_dword v75, v[44:45], off nt
	v_add_co_u32_e32 v0, vcc, s2, v34
	s_mov_b32 s2, 0x15a000
	s_nop 0
	v_addc_co_u32_e32 v1, vcc, 0, v35, vcc
	v_add_co_u32_e32 v28, vcc, s2, v34
	s_mov_b32 s2, 0x160000
	s_nop 0
	v_addc_co_u32_e32 v29, vcc, 0, v35, vcc
	v_add_co_u32_e32 v30, vcc, s2, v34
	s_mov_b32 s2, 0x166000
	s_nop 0
	v_addc_co_u32_e32 v31, vcc, 0, v35, vcc
	v_add_co_u32_e32 v36, vcc, s2, v34
	s_mov_b32 s2, 0x16c000
	s_nop 0
	v_addc_co_u32_e32 v37, vcc, 0, v35, vcc
	global_load_dword v44, v[0:1], off nt
	global_load_dword v45, v[28:29], off nt
	global_load_dword v76, v[30:31], off nt
	global_load_dword v77, v[36:37], off nt
	v_add_co_u32_e32 v0, vcc, s2, v34
	s_mov_b32 s2, 0x172000
	s_nop 0
	v_addc_co_u32_e32 v1, vcc, 0, v35, vcc
	v_add_co_u32_e32 v38, vcc, s2, v34
	s_mov_b32 s2, 0x178000
	s_nop 0
	v_addc_co_u32_e32 v39, vcc, 0, v35, vcc
	v_add_co_u32_e32 v40, vcc, s2, v34
	s_mov_b32 s2, 0x17e000
	s_nop 0
	v_addc_co_u32_e32 v41, vcc, 0, v35, vcc
	v_add_co_u32_e32 v42, vcc, s2, v34
	s_waitcnt vmcnt(35)
	v_fmac_f32_e32 v48, v2, v50
	v_addc_co_u32_e32 v43, vcc, 0, v35, vcc
	global_load_dwordx4 v[28:31], v33, s[0:1] offset:224
	global_load_dword v78, v[0:1], off nt
	global_load_dword v79, v[38:39], off nt
	global_load_dword v80, v[40:41], off nt
	global_load_dword v81, v[42:43], off nt
	global_load_dwordx4 v[34:37], v33, s[0:1] offset:240
	s_waitcnt vmcnt(40)
	v_fmac_f32_e32 v49, v3, v51
	s_waitcnt vmcnt(36)
	v_fmac_f32_e32 v46, v4, v52
	s_waitcnt vmcnt(35)
	v_fmac_f32_e32 v47, v5, v53
	s_waitcnt vmcnt(34)
	v_fmac_f32_e32 v48, v6, v54
	s_waitcnt vmcnt(33)
	v_fmac_f32_e32 v49, v7, v55
	s_waitcnt vmcnt(32)
	v_fmac_f32_e32 v46, v12, v56
	s_waitcnt vmcnt(31)
	v_fmac_f32_e32 v47, v13, v57
	s_waitcnt vmcnt(30)
	v_fmac_f32_e32 v48, v14, v58
	s_waitcnt vmcnt(29)
	v_fmac_f32_e32 v49, v15, v59
	s_waitcnt vmcnt(28)
	v_fmac_f32_e32 v46, v8, v60
	s_waitcnt vmcnt(27)
	v_fmac_f32_e32 v47, v9, v61
	s_waitcnt vmcnt(26)
	v_fmac_f32_e32 v48, v10, v62
	s_waitcnt vmcnt(25)
	v_fmac_f32_e32 v49, v11, v63
	s_waitcnt vmcnt(19)
	v_fmac_f32_e32 v46, v20, v64
	v_fmac_f32_e32 v47, v21, v65
	v_fmac_f32_e32 v48, v22, v66
	v_fmac_f32_e32 v49, v23, v67
	v_lshl_add_u64 v[0:1], s[6:7], 0, v[32:33]
	v_add_co_u32_e32 v0, vcc, 0xd05c000, v0
	s_waitcnt vmcnt(17)
	v_fmac_f32_e32 v46, v24, v68
	s_waitcnt vmcnt(16)
	v_fmac_f32_e32 v47, v25, v69
	s_waitcnt vmcnt(15)
	v_fmac_f32_e32 v48, v26, v70
	s_waitcnt vmcnt(14)
	v_fmac_f32_e32 v49, v27, v71
	s_waitcnt vmcnt(13)
	v_fmac_f32_e32 v46, v16, v72
	s_waitcnt vmcnt(12)
	v_fmac_f32_e32 v47, v17, v73
	s_waitcnt vmcnt(11)
	v_fmac_f32_e32 v48, v18, v74
	s_waitcnt vmcnt(10)
	v_fmac_f32_e32 v49, v19, v75
	v_addc_co_u32_e32 v1, vcc, 0, v1, vcc
	s_waitcnt vmcnt(5)
	v_fmac_f32_e32 v46, v28, v44
	v_fmac_f32_e32 v47, v29, v45
	v_fmac_f32_e32 v48, v30, v76
	v_fmac_f32_e32 v49, v31, v77
	s_waitcnt vmcnt(0)
	v_fmac_f32_e32 v46, v34, v78
	v_fmac_f32_e32 v47, v35, v79
	v_fmac_f32_e32 v48, v36, v80
	v_fmac_f32_e32 v49, v37, v81
	v_add_f32_e32 v2, v47, v46
	v_add_f32_e32 v3, v49, v48
	v_add_f32_e32 v2, v3, v2
	global_atomic_add_f32 v[0:1], v2, off
	s_endpgm
	.p2align	8

_ZN2rb6k_gemmILi2ENS_7SchedP1ENS_5EpiP1EEEvT0_T1_:
	s_load_dwordx4 s[80:83], s[0:1], 0x28
	s_load_dwordx4 s[84:87], s[0:1], 0x38
	s_load_dwordx2 s[88:89], s[0:1], 0x50
	s_ashr_i32 s3, s2, 31
	s_lshr_b32 s3, s3, 29
	s_add_i32 s6, s2, s3
	s_and_b32 s3, s6, -8
	s_sub_i32 s20, s2, s3
	s_cmp_gt_i32 s20, -1
	s_cselect_b64 s[10:11], -1, 0
	v_readfirstlane_b32 s33, v0
	s_and_b64 vcc, exec, s[10:11]
	s_cbranch_vccz .LBB2_2
	s_lshl_b32 s3, s20, 5
	s_ashr_i32 s15, s6, 3
	s_mul_i32 s6, s20, 33
	s_cbranch_execz .LBB2_3
	s_branch .LBB2_4

.LBB2_8:
	v_lshlrev_b32_e32 v2, 2, v0
	s_add_u32 s16, s0, 24
	v_lshrrev_b32_e32 v1, 6, v0
	v_and_b32_e32 v2, 0xfc, v2
	s_addc_u32 s17, s1, 0
	s_movk_i32 s4, 0xc0
	v_cmp_eq_u32_e64 s[8:9], 1, v1
	v_lshlrev_b32_e32 v1, 10, v1
	s_add_i32 s12, 0, 0x20000
	v_lshlrev_b32_e32 v2, 2, v2
	v_cmp_gt_u32_e64 s[6:7], s4, v0
	v_cmp_gt_u32_e64 s[4:5], 64, v0
	v_mov_b32_e32 v5, 0
	v_add3_u32 v1, s12, v1, v2
	v_mov_b32_e32 v32, v1
	s_mov_b64 s[90:91], s[6:7]
	s_and_saveexec_b64 s[12:13], s[6:7]
	s_cbranch_execz .LBB2_10
	s_add_i32 s23, s23, s15
	s_ashr_i32 s24, s23, 31
	s_lshr_b32 s24, s24, 26
	s_add_i32 s24, s23, s24
	s_ashr_i32 s25, s24, 6
	s_lshl_b32 s25, s25, 3
	s_sub_i32 s26, 32, s25
	s_min_i32 s26, s26, 8
	s_abs_i32 s27, s26
	v_cvt_f32_u32_e32 v3, s27
	s_sub_i32 s29, 0, s27
	s_andn2_b32 s24, s24, 63
	s_sub_i32 s23, s23, s24
	v_rcp_iflag_f32_e32 v3, v3
	s_abs_i32 s24, s23
	s_xor_b32 s28, s23, s26
	s_ashr_i32 s28, s28, 31
	v_mul_f32_e32 v3, 0x4f7ffffe, v3
	v_cvt_u32_f32_e32 v3, v3
	s_nop 0
	v_readfirstlane_b32 s30, v3
	s_mul_i32 s29, s29, s30
	s_mul_hi_u32 s29, s30, s29
	s_add_i32 s30, s30, s29
	s_mul_hi_u32 s29, s24, s30
	s_mul_i32 s30, s29, s27
	s_sub_i32 s24, s24, s30
	s_add_i32 s31, s29, 1
	s_sub_i32 s30, s24, s27
	s_cmp_ge_u32 s24, s27
	s_cselect_b32 s29, s31, s29
	s_cselect_b32 s24, s30, s24
	s_add_i32 s30, s29, 1
	s_cmp_ge_u32 s24, s27
	s_cselect_b32 s24, s30, s29
	s_xor_b32 s24, s24, s28
	s_sub_i32 s24, s24, s28
	s_mul_i32 s26, s24, s26
	s_sub_i32 s23, s23, s26
	s_add_i32 s23, s23, s25
	v_mov_b32_e32 v3, s24
	v_mov_b32_e32 v4, s23
	s_or_b64 vcc, s[4:5], s[8:9]
	v_cndmask_b32_e32 v3, v4, v3, vcc
	v_lshlrev_b32_e32 v8, 8, v3
	v_ashrrev_i32_e32 v9, 31, v8
	v_mov_b32_e32 v3, v5
	s_waitcnt lgkmcnt(0)
	v_mov_b32_e32 v6, s88
	v_mov_b32_e32 v7, s89
	v_mov_b32_e32 v10, s82
	v_mov_b32_e32 v11, s83
	v_cndmask_b32_e64 v6, v6, v10, s[8:9]
	v_cndmask_b32_e64 v7, v7, v11, s[8:9]
	v_mov_b32_e32 v10, s80
	v_mov_b32_e32 v11, s81
	v_cndmask_b32_e64 v6, v6, v10, s[4:5]
	v_cndmask_b32_e64 v7, v7, v11, s[4:5]
	v_lshl_add_u64 v[6:7], v[8:9], 2, v[6:7]
	v_lshl_add_u64 v[4:5], v[6:7], 0, v[2:3]
	global_load_dwordx4 v[20:23], v[4:5], off

.LBB2_14:
	s_sub_i32 s20, s21, s22
	s_add_u32 s21, s16, 32
	s_mul_hi_u32 s12, s14, s12
	s_addc_u32 s22, s17, 0
	v_cndmask_b32_e64 v4, 56, 40, s[8:9]
	s_and_saveexec_b64 s[10:11], s[6:7]
	s_cbranch_execz .LBB2_16
	v_mov_b32_e32 v5, 0
	s_add_i32 s13, s13, s15
	s_ashr_i32 s15, s13, 31
	s_lshr_b32 s15, s15, 24
	s_add_i32 s15, s13, s15
	s_ashr_i32 s23, s15, 8
	s_lshl_b32 s23, s23, 3
	s_sub_i32 s24, 16, s23
	s_min_i32 s24, s24, 8
	s_abs_i32 s25, s24
	v_cvt_f32_u32_e32 v3, s25
	s_sub_i32 s27, 0, s25
	s_and_b32 s15, s15, 0xffffff00
	s_sub_i32 s13, s13, s15
	v_rcp_iflag_f32_e32 v3, v3
	s_abs_i32 s15, s13
	s_xor_b32 s26, s13, s24
	s_ashr_i32 s26, s26, 31
	v_mul_f32_e32 v3, 0x4f7ffffe, v3
	v_cvt_u32_f32_e32 v3, v3
	s_nop 0
	v_readfirstlane_b32 s28, v3
	s_mul_i32 s27, s27, s28
	s_mul_hi_u32 s27, s28, s27
	s_add_i32 s28, s28, s27
	s_mul_hi_u32 s27, s15, s28
	s_mul_i32 s28, s27, s25
	s_sub_i32 s15, s15, s28
	s_add_i32 s29, s27, 1
	s_sub_i32 s28, s15, s25
	s_cmp_ge_u32 s15, s25
	s_cselect_b32 s27, s29, s27
	s_cselect_b32 s15, s28, s15
	s_add_i32 s28, s27, 1
	s_cmp_ge_u32 s15, s25
	s_cselect_b32 s15, s28, s27
	s_xor_b32 s15, s15, s26
	s_sub_i32 s15, s15, s26
	s_mul_i32 s24, s15, s24
	s_sub_i32 s13, s13, s24
	s_add_i32 s13, s13, s23
	v_mov_b32_e32 v3, s15
	v_mov_b32_e32 v8, s13
	s_or_b64 vcc, s[4:5], s[8:9]
	v_cndmask_b32_e32 v3, v3, v8, vcc
	v_lshlrev_b32_e32 v8, 8, v3
	v_ashrrev_i32_e32 v9, 31, v8
	v_mov_b32_e32 v3, v5
	s_waitcnt lgkmcnt(0)
	v_mov_b32_e32 v6, s88
	v_mov_b32_e32 v7, s89
	v_mov_b32_e32 v10, s86
	v_mov_b32_e32 v11, s87
	v_cndmask_b32_e64 v6, v6, v10, s[8:9]
	v_cndmask_b32_e64 v7, v7, v11, s[8:9]
	v_mov_b32_e32 v10, s84
	v_mov_b32_e32 v11, s85
	v_cndmask_b32_e64 v6, v6, v10, s[4:5]
	v_cndmask_b32_e64 v7, v7, v11, s[4:5]
	v_lshl_add_u64 v[6:7], v[8:9], 2, v[6:7]
	v_lshl_add_u64 v[6:7], v[6:7], 0, v[2:3]
	global_load_dwordx4 v[24:27], v[6:7], off

.LBB2_20:
	s_load_dwordx4 s[12:15], s[0:1], 0x0
	s_ashr_i32 s11, s20, 31
	s_ashr_i32 s24, s18, 31
	s_and_saveexec_b64 s[0:1], s[6:7]
	s_cbranch_execz .LBB2_22
	v_mov_b32_e32 v5, 0
	s_ashr_i32 s6, s25, 3
	s_add_i32 s6, s26, s6
	s_ashr_i32 s7, s6, 31
	s_lshr_b32 s7, s7, 24
	s_add_i32 s7, s6, s7
	s_ashr_i32 s21, s7, 8
	s_lshl_b32 s21, s21, 3
	s_sub_i32 s22, 16, s21
	s_min_i32 s22, s22, 8
	s_abs_i32 s25, s22
	v_cvt_f32_u32_e32 v3, s25
	s_sub_i32 s27, 0, s25
	s_and_b32 s7, s7, 0xffffff00
	s_sub_i32 s6, s6, s7
	v_rcp_iflag_f32_e32 v3, v3
	s_abs_i32 s7, s6
	s_xor_b32 s26, s6, s22
	s_ashr_i32 s26, s26, 31
	v_mul_f32_e32 v3, 0x4f7ffffe, v3
	v_cvt_u32_f32_e32 v3, v3
	s_nop 0
	v_readfirstlane_b32 s28, v3
	s_mul_i32 s27, s27, s28
	s_mul_hi_u32 s27, s28, s27
	s_add_i32 s28, s28, s27
	s_mul_hi_u32 s27, s7, s28
	s_mul_i32 s28, s27, s25
	s_sub_i32 s7, s7, s28
	s_add_i32 s29, s27, 1
	s_sub_i32 s28, s7, s25
	s_cmp_ge_u32 s7, s25
	s_cselect_b32 s27, s29, s27
	s_cselect_b32 s7, s28, s7
	s_add_i32 s28, s27, 1
	s_cmp_ge_u32 s7, s25
	s_cselect_b32 s7, s28, s27
	s_xor_b32 s7, s7, s26
	s_sub_i32 s7, s7, s26
	s_mul_i32 s22, s7, s22
	s_sub_i32 s6, s6, s22
	s_add_i32 s6, s6, s21
	v_mov_b32_e32 v3, s7
	v_mov_b32_e32 v4, s6
	s_or_b64 vcc, s[4:5], s[8:9]
	v_cndmask_b32_e32 v3, v3, v4, vcc
	v_lshlrev_b32_e32 v8, 8, v3
	v_ashrrev_i32_e32 v9, 31, v8
	v_mov_b32_e32 v3, v5
	s_waitcnt lgkmcnt(0)
	v_mov_b32_e32 v6, s88
	v_mov_b32_e32 v7, s89
	v_mov_b32_e32 v10, s86
	v_mov_b32_e32 v11, s87
	v_cndmask_b32_e64 v6, v6, v10, s[8:9]
	v_cndmask_b32_e64 v7, v7, v11, s[8:9]
	v_mov_b32_e32 v10, s84
	v_mov_b32_e32 v11, s85
	v_cndmask_b32_e64 v6, v6, v10, s[4:5]
	v_cndmask_b32_e64 v7, v7, v11, s[4:5]
	v_lshl_add_u64 v[6:7], v[8:9], 2, v[6:7]
	v_lshl_add_u64 v[2:3], v[6:7], 0, v[2:3]
	global_load_dwordx4 v[28:31], v[2:3], off
.LBB2_22:
	s_or_b64 exec, exec, s[0:1]
	s_mul_i32 s1, s10, s19
	s_sub_i32 s1, s23, s1
	s_xor_b32 s0, s11, s24
	s_add_i32 s4, s10, 1
	s_sub_i32 s5, s1, s19
	s_cmp_ge_u32 s1, s19
	s_cselect_b32 s4, s4, s10
	s_cselect_b32 s1, s5, s1
	s_add_i32 s5, s4, 1
	s_cmp_ge_u32 s1, s19
	s_cselect_b32 s1, s5, s4
	s_xor_b32 s1, s1, s0
	s_sub_i32 s64, s1, s0
	s_mul_i32 s0, s64, s18
	s_sub_i32 s0, s20, s0
	s_add_i32 s23, s3, s0
	v_lshlrev_b32_e32 v1, 4, v0
	s_movk_i32 s0, 0x70
	v_lshrrev_b32_e32 v3, 5, v0
	v_bitop3_b32 v2, v1, s0, v0 bitop3:0x48
	v_and_b32_e32 v3, 4, v3
	v_lshrrev_b32_e32 v4, 3, v0
	v_or_b32_e32 v1, 0x2000, v1
	v_and_or_b32 v3, v4, 3, v3
	v_lshl_or_b32 v193, v4, 11, v2
	v_lshrrev_b32_e32 v4, 6, v1
	v_lshlrev_b32_e32 v1, 4, v1
	s_mov_b32 s0, 0x3f800
	v_and_or_b32 v197, v1, s0, v2
	s_lshl_b32 s0, s23, 8
	s_ashr_i32 s1, s0, 31
	s_lshl_b64 s[10:11], s[0:1], 11
	s_lshl_b32 s0, s64, 8
	s_lshr_b32 s8, s33, 6
	s_ashr_i32 s1, s0, 31
	s_lshr_b32 s3, s33, 8
	s_lshl_b32 s9, s8, 10
	s_lshl_b64 s[0:1], s[0:1], 11
	v_lshrrev_b32_e32 v5, 2, v0
	v_lshrrev_b32_e32 v6, 1, v0
	s_waitcnt lgkmcnt(0)
	s_add_u32 s0, s14, s0
	v_and_b32_e32 v5, 64, v5
	v_and_b32_e32 v6, 48, v6
	s_addc_u32 s1, s15, s1
	s_add_i32 s38, s9, 0
	v_or3_b32 v5, v6, v5, v3
	v_and_b32_e32 v4, 0xc0, v4
	s_and_b32 s5, s1, 0xffff
	s_add_i32 s39, s38, 0x10000
	s_add_i32 s40, s38, 0x12000
	v_lshl_or_b32 v196, v5, 11, v2
	v_or3_b32 v3, v6, v4, v3
	s_mov_b32 s7, 0x20000
	s_mov_b32 s6, -1
	s_mov_b32 s4, s0
	s_mov_b32 m0, s39
	s_add_u32 s18, s12, s10
	v_lshl_or_b32 v198, v3, 11, v2
	buffer_load_dwordx4 v196, s[4:7], 0 offen lds
	s_mov_b32 m0, s40
	s_addc_u32 s19, s13, s11
	buffer_load_dwordx4 v198, s[4:7], 0 offen lds
	s_and_b32 s5, s19, 0xffff
	s_mov_b32 s4, s18
	s_mov_b32 m0, s38
	s_add_i32 s41, s38, 0x2000
	buffer_load_dwordx4 v193, s[4:7], 0 offen lds
	s_mov_b32 m0, s41
	s_mov_b32 s65, 0
	buffer_load_dwordx4 v197, s[4:7], 0 offen lds
	s_add_u32 s4, s0, 0x4000
	s_addc_u32 s5, s1, 0
	s_add_i32 s42, s38, 0x14000
	s_and_b32 s5, s5, 0xffff
	s_mov_b32 m0, s42
	s_add_i32 s43, s38, 0x16000
	buffer_load_dwordx4 v196, s[4:7], 0 offen lds
	s_mov_b32 m0, s43
	s_nop 0
	buffer_load_dwordx4 v198, s[4:7], 0 offen lds
	s_add_u32 s4, s18, 0x40000
	s_addc_u32 s5, s19, 0
	s_add_i32 s44, s38, 0x4000
	s_and_b32 s5, s5, 0xffff
	s_mov_b32 m0, s44
	s_add_i32 s45, s38, 0x6000
	buffer_load_dwordx4 v193, s[4:7], 0 offen lds
	s_mov_b32 m0, s45
	s_cmp_lg_u32 s3, 1
	buffer_load_dwordx4 v197, s[4:7], 0 offen lds
	s_cbranch_scc1 .LBB2_24
	s_barrier
.LBB2_24:
	s_and_b32 s46, s8, 3
	s_add_u32 s4, s0, 0x80
	s_addc_u32 s5, s1, 0
	s_add_i32 s47, s38, 0x18000
	s_and_b32 s5, s5, 0xffff
	s_mov_b32 m0, s47
	s_add_i32 s48, s38, 0x1a000
	s_waitcnt vmcnt(4)
	s_and_saveexec_b64 s[92:93], s[90:91]
	s_cbranch_execz .Lp1_par_done
	ds_write_b128 v32, v[20:23]
	ds_write_b128 v32, v[24:27] offset:3072
	ds_write_b128 v32, v[28:31] offset:6144
	s_waitcnt lgkmcnt(0)
.Lp1_par_done:
	s_or_b64 exec, exec, s[92:93]
	s_barrier
	buffer_load_dwordx4 v196, s[4:7], 0 offen lds
	s_mov_b32 m0, s48
	v_lshrrev_b32_e32 v1, 4, v0
	buffer_load_dwordx4 v198, s[4:7], 0 offen lds
	s_add_u32 s4, s18, 0x80
	s_addc_u32 s5, s19, 0
	s_add_i32 s49, s38, 0x8000
	s_and_b32 s5, s5, 0xffff
	s_mov_b32 m0, s49
	s_add_i32 s50, s38, 0xa000
	buffer_load_dwordx4 v193, s[4:7], 0 offen lds
	s_mov_b32 m0, s50
	v_and_b32_e32 v2, 15, v0
	buffer_load_dwordx4 v197, s[4:7], 0 offen lds
	s_add_u32 s4, s0, 0x4080
	s_addc_u32 s5, s1, 0
	s_add_i32 s51, s38, 0x1c000
	s_and_b32 s5, s5, 0xffff
	s_mov_b32 m0, s51
	s_add_i32 s52, s38, 0x1e000
	buffer_load_dwordx4 v196, s[4:7], 0 offen lds
	s_mov_b32 m0, s52
	v_bfe_u32 v3, v0, 4, 2
	buffer_load_dwordx4 v198, s[4:7], 0 offen lds
	v_bfe_u32 v0, v0, 1, 3
	v_bitop3_b32 v0, v1, v0, 3 bitop3:0x6c
	v_lshlrev_b32_e32 v1, 7, v2
	v_lshl_or_b32 v4, s3, 13, v1
	s_waitcnt vmcnt(6)
	s_barrier
	v_lshl_or_b32 v201, s3, 6, v2
	s_add_i32 s55, s2, 0xffffff00
	s_load_dwordx4 s[8:11], s[16:17], 0x0
	s_load_dwordx2 s[2:3], s[16:17], 0x30
	v_lshlrev_b32_e32 v0, 4, v0
	v_lshl_or_b32 v1, s46, 12, v1
	v_or_b32_e32 v199, v1, v0
	v_bitop3_b32 v200, v1, 64, v0 bitop3:0x36
	s_add_i32 s16, 0, 0x10000
	v_or_b32_e32 v5, v4, v0
	v_bitop3_b32 v4, v4, 64, v0 bitop3:0x36
	v_lshlrev_b32_e32 v0, 4, v3
	v_add_u32_e32 v203, s16, v199
	v_add_u32_e32 v204, s16, v200
	s_add_i32 s16, 0, 0x14000
	s_add_i32 s53, s38, 0xc000
	v_lshl_or_b32 v202, s46, 6, v0
	v_cmp_eq_u32_e64 s[20:21], 0, v2
	v_lshlrev_b32_e32 v192, 2, v3
	v_mov_b32_e32 v195, 0
	s_add_i32 s54, s38, 0xe000
	s_mov_b64 s[4:5], -1
	v_add_u32_e32 v205, 0, v5
	v_add_u32_e32 v206, 0, v4
	v_add_u32_e32 v207, s16, v199
	v_add_u32_e32 v208, s16, v200
	s_mov_b32 s22, 0x38383838
	s_mov_b32 s56, 0x100000
	s_mov_b32 s57, 0x140000
	s_mov_b32 s58, 0x40000
	s_mov_b32 s59, 0x48000
	s_mov_b32 s60, 0x50000
	s_branch .LBB2_26

.LBB2_90:
	s_barrier
	s_endpgm
	.p2align	8

	.amdhsa_kernel _ZN2rb6k_gemmILi2ENS_7SchedP1ENS_5EpiP1EEEvT0_T1_
		.amdhsa_group_segment_fixed_size 0
		.amdhsa_private_segment_fixed_size 0
		.amdhsa_kernarg_size 88
		.amdhsa_user_sgpr_count 2
		.amdhsa_user_sgpr_dispatch_ptr 0
		.amdhsa_user_sgpr_queue_ptr 0
		.amdhsa_user_sgpr_kernarg_segment_ptr 1
		.amdhsa_user_sgpr_dispatch_id 0
		.amdhsa_user_sgpr_kernarg_preload_length 0
		.amdhsa_user_sgpr_kernarg_preload_offset 0
		.amdhsa_user_sgpr_private_segment_size 0
		.amdhsa_uses_dynamic_stack 0
		.amdhsa_enable_private_segment 0
		.amdhsa_system_sgpr_workgroup_id_x 1
		.amdhsa_system_sgpr_workgroup_id_y 0
		.amdhsa_system_sgpr_workgroup_id_z 0
		.amdhsa_system_sgpr_workgroup_info 0
		.amdhsa_system_vgpr_workitem_id 0
		.amdhsa_next_free_vgpr 209
		.amdhsa_next_free_sgpr 94
		.amdhsa_accum_offset 212
		.amdhsa_reserve_vcc 1
		.amdhsa_float_round_mode_32 0
		.amdhsa_float_round_mode_16_64 0
		.amdhsa_float_denorm_mode_32 3
		.amdhsa_float_denorm_mode_16_64 3
		.amdhsa_dx10_clamp 1
		.amdhsa_ieee_mode 1
		.amdhsa_fp16_overflow 0
		.amdhsa_tg_split 0
		.amdhsa_exception_fp_ieee_invalid_op 0
		.amdhsa_exception_fp_denorm_src 0
		.amdhsa_exception_fp_ieee_div_zero 0
		.amdhsa_exception_fp_ieee_overflow 0
		.amdhsa_exception_fp_ieee_underflow 0
		.amdhsa_exception_fp_ieee_inexact 0
		.amdhsa_exception_int_div_zero 0
	.end_amdhsa_kernel

	.text
	.p2alignl 8, 3212836864
	.fill 256, 4, 3212836864

amdhsa.kernels:
  - .agpr_count:     0
    .args:
      - .actual_access:  read_only
        .address_space:  global
        .offset:         0
        .size:           8
        .value_kind:     global_buffer
      - .actual_access:  read_only
        .address_space:  global
        .offset:         8
        .size:           8
        .value_kind:     global_buffer
      - .actual_access:  read_only
        .address_space:  global
        .offset:         16
        .size:           8
        .value_kind:     global_buffer
      - .actual_access:  read_only
        .address_space:  global
        .offset:         24
        .size:           8
        .value_kind:     global_buffer
      - .actual_access:  read_only
        .address_space:  global
        .offset:         32
        .size:           8
        .value_kind:     global_buffer
      - .actual_access:  read_only
        .address_space:  global
        .offset:         40
        .size:           8
        .value_kind:     global_buffer
      - .actual_access:  read_only
        .address_space:  global
        .offset:         48
        .size:           8
        .value_kind:     global_buffer
      - .actual_access:  read_only
        .address_space:  global
        .offset:         56
        .size:           8
        .value_kind:     global_buffer
      - .actual_access:  write_only
        .address_space:  global
        .offset:         64
        .size:           8
        .value_kind:     global_buffer
      - .offset:         72
        .size:           4
        .value_kind:     by_value
    .group_segment_fixed_size: 32768
    .kernarg_segment_align: 8
    .kernarg_segment_size: 76
    .language:       OpenCL C
    .language_version:
      - 2
      - 0
    .max_flat_workgroup_size: 256
    .name:           _ZN2rb6k_prepEPKfS1_S1_S1_S1_S1_S1_S1_Phi
    .private_segment_fixed_size: 0
    .sgpr_count:     22
    .sgpr_spill_count: 0
    .symbol:         _ZN2rb6k_prepEPKfS1_S1_S1_S1_S1_S1_S1_Phi.kd
    .uniform_work_group_size: 1
    .uses_dynamic_stack: false
    .vgpr_count:     100
    .vgpr_spill_count: 0
    .wavefront_size: 64
  - .agpr_count:     0
    .args:
      - .address_space:  global
        .offset:         0
        .size:           8
        .value_kind:     global_buffer
      - .actual_access:  read_only
        .address_space:  global
        .offset:         8
        .size:           8
        .value_kind:     global_buffer
    .group_segment_fixed_size: 0
    .kernarg_segment_align: 8
    .kernarg_segment_size: 16
    .language:       OpenCL C
    .language_version:
      - 2
      - 0
    .max_flat_workgroup_size: 256
    .name:           _ZN2rb5k_midEPhPKf
    .private_segment_fixed_size: 0
    .sgpr_count:     20
    .sgpr_spill_count: 0
    .symbol:         _ZN2rb5k_midEPhPKf.kd
    .uniform_work_group_size: 1
    .uses_dynamic_stack: false
    .vgpr_count:     86
    .vgpr_spill_count: 0
    .wavefront_size: 64
  - .agpr_count:     0
    .args:
      - .offset:         0
        .size:           24
        .value_kind:     by_value
      - .offset:         24
        .size:           64
        .value_kind:     by_value
    .group_segment_fixed_size: 0
    .kernarg_segment_align: 8
    .kernarg_segment_size: 88
    .language:       OpenCL C
    .language_version:
      - 2
      - 0
    .max_flat_workgroup_size: 512
    .name:           _ZN2rb6k_gemmILi2ENS_7SchedP1ENS_5EpiP1EEEvT0_T1_
    .private_segment_fixed_size: 0
    .sgpr_count:     100
    .sgpr_spill_count: 0
    .symbol:         _ZN2rb6k_gemmILi2ENS_7SchedP1ENS_5EpiP1EEEvT0_T1_.kd
    .uniform_work_group_size: 1
    .uses_dynamic_stack: false
    .vgpr_count:     209
    .vgpr_spill_count: 0
    .wavefront_size: 64
  - .agpr_count:     0
    .args:
      - .offset:         0
        .size:           24
        .value_kind:     by_value
      - .offset:         24
        .size:           16
        .value_kind:     by_value
    .group_segment_fixed_size: 0
    .kernarg_segment_align: 8
    .kernarg_segment_size: 40
    .language:       OpenCL C
    .language_version:
      - 2
      - 0
    .max_flat_workgroup_size: 512
    .name:           _ZN2rb6k_gemmILi1ENS_7SchedP2ENS_7EpiSlabEEEvT0_T1_
    .private_segment_fixed_size: 0
    .sgpr_count:     66
    .sgpr_spill_count: 0
    .symbol:         _ZN2rb6k_gemmILi1ENS_7SchedP2ENS_7EpiSlabEEEvT0_T1_.kd
    .uniform_work_group_size: 1
    .uses_dynamic_stack: false
    .vgpr_count:     208
    .vgpr_spill_count: 0
    .wavefront_size: 64
  - .agpr_count:     0
    .args:
      - .offset:         0
        .size:           32
        .value_kind:     by_value
      - .offset:         32
        .size:           16
        .value_kind:     by_value
    .group_segment_fixed_size: 0
    .kernarg_segment_align: 8
    .kernarg_segment_size: 48
    .language:       OpenCL C
    .language_version:
      - 2
      - 0
    .max_flat_workgroup_size: 512
    .name:           _ZN2rb6k_gemmILi1ENS_6SchedGILb1EEENS_5EpiP3EEEvT0_T1_
    .private_segment_fixed_size: 0
    .sgpr_count:     62
    .sgpr_spill_count: 0
    .symbol:         _ZN2rb6k_gemmILi1ENS_6SchedGILb1EEENS_5EpiP3EEEvT0_T1_.kd
    .uniform_work_group_size: 1
    .uses_dynamic_stack: false
    .vgpr_count:     207
    .vgpr_spill_count: 0
    .wavefront_size: 64
  - .agpr_count:     0
    .args:
      - .offset:         0
        .size:           32
        .value_kind:     by_value
      - .offset:         32
        .size:           48
        .value_kind:     by_value
    .group_segment_fixed_size: 0
    .kernarg_segment_align: 8
    .kernarg_segment_size: 80
    .language:       OpenCL C
    .language_version:
      - 2
      - 0
    .max_flat_workgroup_size: 512
    .name:           _ZN2rb6k_gemmILi1ENS_6SchedGILb1EEENS_6EpiOutEEEvT0_T1_
    .private_segment_fixed_size: 0
    .sgpr_count:     62
    .sgpr_spill_count: 0
    .symbol:         _ZN2rb6k_gemmILi1ENS_6SchedGILb1EEENS_6EpiOutEEEvT0_T1_.kd
    .uniform_work_group_size: 1
    .uses_dynamic_stack: false
    .vgpr_count:     205
    .vgpr_spill_count: 0
    .wavefront_size: 64
  - .agpr_count:     0
    .args:
      - .offset:         0
        .size:           24
        .value_kind:     by_value
      - .offset:         24
        .size:           1
        .value_kind:     by_value
    .group_segment_fixed_size: 0
    .kernarg_segment_align: 8
    .kernarg_segment_size: 28
    .language:       OpenCL C
    .language_version:
      - 2
      - 0
    .max_flat_workgroup_size: 512
    .name:           _ZN2rb6k_gemmILi2ENS_7SchedP1ENS_7EpiNullEEEvT0_T1_
    .private_segment_fixed_size: 0
    .sgpr_count:     66
    .sgpr_spill_count: 0
    .symbol:         _ZN2rb6k_gemmILi2ENS_7SchedP1ENS_7EpiNullEEEvT0_T1_.kd
    .uniform_work_group_size: 1
    .uses_dynamic_stack: false
    .vgpr_count:     205
    .vgpr_spill_count: 0
    .wavefront_size: 64
